# wconv streaming loads marked sc1 nt
# speedup vs baseline: 1.0147x; 1.0043x over previous
.Lwc_work:
	s_load_dword s8, s[0:1], 0x150
	s_cmp_eq_u32 s3, 5
	s_cselect_b32 s9, 13, 11
	s_cmp_eq_u32 s3, 6
	s_cselect_b32 s10, 13, 11
	s_sub_u32 s11, s9, 7
	s_lshr_b32 s12, s4, s11
	s_lshl_b32 s13, s12, s11
	s_sub_u32 s13, s4, s13
	s_add_u32 s20, s9, 2
	s_add_u32 s21, s10, 1
	v_lshrrev_b32_e32 v4, 5, v0
	v_and_b32_e32 v6, 31, v0
	v_lshlrev_b32_e32 v5, 4, v4
	v_lshlrev_b32_e32 v5, s20, v5
	v_lshl_add_u32 v1, v6, 4, v5
	v_lshlrev_b32_e32 v7, 1, v4
	v_and_b32_e32 v8, 7, v6
	v_xor_b32_e32 v7, v7, v8
	v_lshlrev_b32_e32 v7, 4, v7
	v_lshl_add_u32 v2, v6, 10, v7
	v_xor_b32_e32 v3, 16, v2
	v_lshrrev_b32_e32 v9, 4, v0
	v_and_b32_e32 v10, 15, v0
	v_lshrrev_b32_e32 v11, 6, v0
	v_xor_b32_e32 v11, v10, v11
	v_lshlrev_b32_e32 v11, 4, v11
	v_lshl_add_u32 v84, v9, 8, v11
	v_xor_b32_e32 v85, 64, v84
	v_lshlrev_b32_e32 v12, s21, v9
	v_lshl_add_u32 v86, v10, 4, v12
	s_add_u32 s22, s20, 7
	s_lshl_b32 s23, s12, s22
	s_lshl_b32 s24, s13, 9
	s_add_u32 s23, s23, s24
	s_lshl_b32 s25, 1, s20
	s_add_u32 s26, s21, 7
	s_lshl_b32 s27, s13, s26
	s_lshl_b32 s28, s12, 8
	s_add_u32 s27, s27, s28
	s_add_u32 s29, s10, 5
	s_lshl_b32 s29, 1, s29
	s_waitcnt lgkmcnt(0)
	s_add_u32 s8, s8, s3
	s_lshl_b32 s8, s8, 3
	s_add_u32 s14, s0, s8
	s_addc_u32 s15, s1, 0
	s_load_dwordx2 s[16:17], s[14:15], 0x0
	s_load_dwordx2 s[18:19], s[14:15], 0x70
	s_waitcnt lgkmcnt(0)
	s_add_u32 s16, s16, s23
	s_addc_u32 s17, s17, 0
	s_add_u32 s18, s18, s27
	s_addc_u32 s19, s19, 0
	global_load_dwordx4 v[4:7], v1, s[16:17] sc1 nt
	s_add_u32 s16, s16, s25
	s_addc_u32 s17, s17, 0
	global_load_dwordx4 v[8:11], v1, s[16:17] sc1 nt
	s_add_u32 s16, s16, s25
	s_addc_u32 s17, s17, 0
	global_load_dwordx4 v[12:15], v1, s[16:17] sc1 nt
	s_add_u32 s16, s16, s25
	s_addc_u32 s17, s17, 0
	global_load_dwordx4 v[16:19], v1, s[16:17] sc1 nt
	s_add_u32 s16, s16, s25
	s_addc_u32 s17, s17, 0
	global_load_dwordx4 v[20:23], v1, s[16:17] sc1 nt
	s_add_u32 s16, s16, s25
	s_addc_u32 s17, s17, 0
	global_load_dwordx4 v[24:27], v1, s[16:17] sc1 nt
	s_add_u32 s16, s16, s25
	s_addc_u32 s17, s17, 0
	global_load_dwordx4 v[28:31], v1, s[16:17] sc1 nt
	s_add_u32 s16, s16, s25
	s_addc_u32 s17, s17, 0
	global_load_dwordx4 v[32:35], v1, s[16:17] sc1 nt
	s_add_u32 s16, s16, s25
	s_addc_u32 s17, s17, 0
	global_load_dwordx4 v[36:39], v1, s[16:17] sc1 nt
	s_add_u32 s16, s16, s25
	s_addc_u32 s17, s17, 0
	global_load_dwordx4 v[40:43], v1, s[16:17] sc1 nt
	s_add_u32 s16, s16, s25
	s_addc_u32 s17, s17, 0
	global_load_dwordx4 v[44:47], v1, s[16:17] sc1 nt
	s_add_u32 s16, s16, s25
	s_addc_u32 s17, s17, 0
	global_load_dwordx4 v[48:51], v1, s[16:17] sc1 nt
	s_add_u32 s16, s16, s25
	s_addc_u32 s17, s17, 0
	global_load_dwordx4 v[52:55], v1, s[16:17] sc1 nt
	s_add_u32 s16, s16, s25
	s_addc_u32 s17, s17, 0
	global_load_dwordx4 v[56:59], v1, s[16:17] sc1 nt
	s_add_u32 s16, s16, s25
	s_addc_u32 s17, s17, 0
	global_load_dwordx4 v[60:63], v1, s[16:17] sc1 nt
	s_add_u32 s16, s16, s25
	s_addc_u32 s17, s17, 0
	global_load_dwordx4 v[64:67], v1, s[16:17] sc1 nt
	s_waitcnt vmcnt(14)
	v_cvt_pk_f16_f32 v68, v4, v8
	v_cvt_pk_f16_f32 v72, v5, v9
	v_cvt_pk_f16_f32 v76, v6, v10
	v_cvt_pk_f16_f32 v80, v7, v11
	s_waitcnt vmcnt(12)
	v_cvt_pk_f16_f32 v69, v12, v16
	v_cvt_pk_f16_f32 v73, v13, v17
	v_cvt_pk_f16_f32 v77, v14, v18
	v_cvt_pk_f16_f32 v81, v15, v19
	s_waitcnt vmcnt(10)
	v_cvt_pk_f16_f32 v70, v20, v24
	v_cvt_pk_f16_f32 v74, v21, v25
	v_cvt_pk_f16_f32 v78, v22, v26
	v_cvt_pk_f16_f32 v82, v23, v27
	s_waitcnt vmcnt(8)
	v_cvt_pk_f16_f32 v71, v28, v32
	v_cvt_pk_f16_f32 v75, v29, v33
	v_cvt_pk_f16_f32 v79, v30, v34
	v_cvt_pk_f16_f32 v83, v31, v35
	ds_write_b128 v2, v[68:71]
	ds_write_b128 v2, v[72:75] offset:256
	ds_write_b128 v2, v[76:79] offset:512
	ds_write_b128 v2, v[80:83] offset:768
	s_waitcnt vmcnt(6)
	v_cvt_pk_f16_f32 v4, v36, v40
	v_cvt_pk_f16_f32 v8, v37, v41
	v_cvt_pk_f16_f32 v12, v38, v42
	v_cvt_pk_f16_f32 v16, v39, v43
	s_waitcnt vmcnt(4)
	v_cvt_pk_f16_f32 v5, v44, v48
	v_cvt_pk_f16_f32 v9, v45, v49
	v_cvt_pk_f16_f32 v13, v46, v50
	v_cvt_pk_f16_f32 v17, v47, v51
	s_waitcnt vmcnt(2)
	v_cvt_pk_f16_f32 v6, v52, v56
	v_cvt_pk_f16_f32 v10, v53, v57
	v_cvt_pk_f16_f32 v14, v54, v58
	v_cvt_pk_f16_f32 v18, v55, v59
	s_waitcnt vmcnt(0)
	v_cvt_pk_f16_f32 v7, v60, v64
	v_cvt_pk_f16_f32 v11, v61, v65
	v_cvt_pk_f16_f32 v15, v62, v66
	v_cvt_pk_f16_f32 v19, v63, v67
	ds_write_b128 v3, v[4:7]
	ds_write_b128 v3, v[8:11] offset:256
	ds_write_b128 v3, v[12:15] offset:512
	ds_write_b128 v3, v[16:19] offset:768
	s_waitcnt lgkmcnt(0)
	s_barrier
	ds_read_b128 v[4:7], v84
	ds_read_b128 v[8:11], v85 offset:4096
	ds_read_b128 v[12:15], v84 offset:8192
	ds_read_b128 v[16:19], v85 offset:12288
	ds_read_b128 v[20:23], v84 offset:16384
	ds_read_b128 v[24:27], v85 offset:20480
	ds_read_b128 v[28:31], v84 offset:24576
	ds_read_b128 v[32:35], v85 offset:28672
	s_waitcnt lgkmcnt(7)
	global_store_dwordx4 v86, v[4:7], s[18:19] sc1
	s_add_u32 s18, s18, s29
	s_addc_u32 s19, s19, 0
	s_waitcnt lgkmcnt(6)
	global_store_dwordx4 v86, v[8:11], s[18:19] sc1
	s_add_u32 s18, s18, s29
	s_addc_u32 s19, s19, 0
	s_waitcnt lgkmcnt(5)
	global_store_dwordx4 v86, v[12:15], s[18:19] sc1
	s_add_u32 s18, s18, s29
	s_addc_u32 s19, s19, 0
	s_waitcnt lgkmcnt(4)
	global_store_dwordx4 v86, v[16:19], s[18:19] sc1
	s_add_u32 s18, s18, s29
	s_addc_u32 s19, s19, 0
	s_waitcnt lgkmcnt(3)
	global_store_dwordx4 v86, v[20:23], s[18:19] sc1
	s_add_u32 s18, s18, s29
	s_addc_u32 s19, s19, 0
	s_waitcnt lgkmcnt(2)
	global_store_dwordx4 v86, v[24:27], s[18:19] sc1
	s_add_u32 s18, s18, s29
	s_addc_u32 s19, s19, 0
	s_waitcnt lgkmcnt(1)
	global_store_dwordx4 v86, v[28:31], s[18:19] sc1
	s_add_u32 s18, s18, s29
	s_addc_u32 s19, s19, 0
	s_waitcnt lgkmcnt(0)
	global_store_dwordx4 v86, v[32:35], s[18:19] sc1
